# GEMM unit start: first K-tile pair peeled with C=0 first-touch MFMAs (accumulator zeroing removed) for in-proj and out-proj; plus rtab/prologue/prio trims
# speedup vs baseline: 1.0058x; 1.0040x over previous
.LBB0_264:
	s_ashr_i32 s73, s72, 31
	s_lshl_b64 s[26:27], s[72:73], 21
	s_add_u32 s76, s38, s26
	s_addc_u32 s77, s40, s27
	s_and_b64 s[26:27], s[4:5], exec
	s_cselect_b32 s73, s77, s7
	s_cselect_b32 vcc_lo, s76, s6
	s_ashr_i32 s75, s74, 31
	s_lshl_b64 s[26:27], s[74:75], 21
	s_add_u32 s96, s42, s26
	s_addc_u32 s97, s44, s27
	s_and_b64 s[26:27], s[4:5], exec
	s_cselect_b32 s75, s97, s25
	s_cselect_b32 vcc_hi, s96, s24
	s_add_u32 s6, s6, 0x100080
	s_addc_u32 s7, s7, 0
	s_add_u32 s21, s24, 0x100
	s_addc_u32 s13, s25, 0
	s_mov_b32 s58, -2
	s_add_u32 s24, s6, 0xfff00080
	s_addc_u32 s25, s7, -1
	s_add_i32 s28, 0, 0x10000
	s_cmp_eq_u32 s58, 60
	s_cselect_b32 s27, s73, s25
	s_cselect_b32 s26, vcc_lo, s24
	s_cselect_b32 s25, s75, s13
	s_cselect_b32 s24, vcc_hi, s21
	s_add_i32 s71, 0, 0x14000
	v_add_u32_e32 v144, s28, v163
	v_add_u32_e32 v182, s71, v163
	s_waitcnt lgkmcnt(0)
	ds_read_b128 v[132:135], v144
	ds_read_b128 v[136:139], v144 offset:1024
	ds_read_b128 v[140:143], v144 offset:2048
	ds_read_b128 v[144:147], v144 offset:3072
	ds_read_b128 v[148:151], v182
	ds_read_b128 v[152:155], v182 offset:1024
	ds_read_b128 v[178:181], v182 offset:2048
	ds_read_b128 v[186:189], v182 offset:3072
	v_lshl_add_u64 v[182:183], s[6:7], 0, v[174:175]
	s_add_i32 m0, s46, 0xc000
	ds_read_b128 v[190:193], v184
	ds_read_b128 v[194:197], v184 offset:1024
	ds_read_b128 v[198:201], v184 offset:2048
	ds_read_b128 v[202:205], v184 offset:3072
	ds_read_b128 v[222:225], v184 offset:4096
	ds_read_b128 v[226:229], v184 offset:5120
	ds_read_b128 v[230:233], v184 offset:6144
	ds_read_b128 v[234:237], v184 offset:7168
	global_load_lds_dwordx4 v[182:183], off
	v_lshl_add_u64 v[182:183], s[6:7], 0, v[176:177]
	s_add_i32 m0, s46, 0xe000
	s_nop 0
	global_load_lds_dwordx4 v[182:183], off
	s_waitcnt vmcnt(8)
	s_waitcnt lgkmcnt(0)
	s_setprio 1
	s_barrier
	v_mfma_f32_16x16x32_bf16 v[120:123], v[132:135], v[190:193], 0
	v_mfma_f32_16x16x32_bf16 v[116:119], v[140:143], v[190:193], 0
	v_mfma_f32_16x16x32_bf16 v[104:107], v[132:135], v[198:201], 0
	v_mfma_f32_16x16x32_bf16 v[100:103], v[140:143], v[198:201], 0
	v_mfma_f32_16x16x32_bf16 v[88:91], v[132:135], v[222:225], 0
	v_mfma_f32_16x16x32_bf16 v[84:87], v[140:143], v[222:225], 0
	v_mfma_f32_16x16x32_bf16 v[72:75], v[132:135], v[230:233], 0
	v_mfma_f32_16x16x32_bf16 v[68:71], v[140:143], v[230:233], 0
	v_mfma_f32_16x16x32_bf16 v[120:123], v[136:139], v[194:197], v[120:123]
	v_mfma_f32_16x16x32_bf16 v[116:119], v[144:147], v[194:197], v[116:119]
	v_mfma_f32_16x16x32_bf16 v[104:107], v[136:139], v[202:205], v[104:107]
	v_mfma_f32_16x16x32_bf16 v[100:103], v[144:147], v[202:205], v[100:103]
	v_mfma_f32_16x16x32_bf16 v[88:91], v[136:139], v[226:229], v[88:91]
	v_mfma_f32_16x16x32_bf16 v[84:87], v[144:147], v[226:229], v[84:87]
	v_mfma_f32_16x16x32_bf16 v[72:75], v[136:139], v[234:237], v[72:75]
	v_mfma_f32_16x16x32_bf16 v[68:71], v[144:147], v[234:237], v[68:71]
	v_mfma_f32_16x16x32_bf16 v[128:131], v[148:151], v[190:193], 0
	v_mfma_f32_16x16x32_bf16 v[124:127], v[178:181], v[190:193], 0
	v_mfma_f32_16x16x32_bf16 v[112:115], v[148:151], v[198:201], 0
	v_mfma_f32_16x16x32_bf16 v[108:111], v[178:181], v[198:201], 0
	v_mfma_f32_16x16x32_bf16 v[96:99], v[148:151], v[222:225], 0
	v_mfma_f32_16x16x32_bf16 v[92:95], v[178:181], v[222:225], 0
	v_mfma_f32_16x16x32_bf16 v[80:83], v[148:151], v[230:233], 0
	v_mfma_f32_16x16x32_bf16 v[76:79], v[178:181], v[230:233], 0
	v_mfma_f32_16x16x32_bf16 v[128:131], v[152:155], v[194:197], v[128:131]
	v_mfma_f32_16x16x32_bf16 v[124:127], v[186:189], v[194:197], v[124:127]
	v_mfma_f32_16x16x32_bf16 v[112:115], v[152:155], v[202:205], v[112:115]
	v_mfma_f32_16x16x32_bf16 v[108:111], v[186:189], v[202:205], v[108:111]
	v_mfma_f32_16x16x32_bf16 v[96:99], v[152:155], v[226:229], v[96:99]
	v_mfma_f32_16x16x32_bf16 v[92:95], v[186:189], v[226:229], v[92:95]
	v_mfma_f32_16x16x32_bf16 v[80:83], v[152:155], v[234:237], v[80:83]
	v_mfma_f32_16x16x32_bf16 v[76:79], v[186:189], v[234:237], v[76:79]
	s_barrier
	s_setprio 0
	s_add_i32 s28, s28, s1
	v_lshl_add_u64 v[182:183], s[24:25], 0, v[2:3]
	s_mov_b32 m0, s28
	ds_read_b128 v[190:193], v184 offset:16384
	ds_read_b128 v[194:197], v184 offset:17408
	ds_read_b128 v[198:201], v184 offset:18432
	ds_read_b128 v[202:205], v184 offset:19456
	ds_read_b128 v[222:225], v184 offset:20480
	ds_read_b128 v[226:229], v184 offset:21504
	ds_read_b128 v[230:233], v184 offset:22528
	ds_read_b128 v[234:237], v184 offset:23552
	global_load_lds_dwordx4 v[182:183], off
	s_add_i32 m0, s28, 0x2000
	s_add_u32 s28, s24, 0x100000
	v_lshl_add_u64 v[238:239], s[24:25], 0, v[168:169]
	s_addc_u32 s29, s25, 0
	s_add_i32 s71, s71, s1
	global_load_lds_dwordx4 v[238:239], off
	v_lshl_add_u64 v[240:241], s[28:29], 0, v[2:3]
	s_mov_b32 m0, s71
	v_lshl_add_u64 v[242:243], s[26:27], 0, v[170:171]
	global_load_lds_dwordx4 v[240:241], off
	v_lshl_add_u64 v[240:241], s[28:29], 0, v[168:169]
	s_add_i32 m0, s71, 0x2000
	s_nop 0
	global_load_lds_dwordx4 v[240:241], off
	v_lshl_add_u64 v[240:241], s[26:27], 0, v[172:173]
	s_mov_b32 m0, s46
	s_nop 0
	global_load_lds_dwordx4 v[240:241], off
	s_mov_b32 m0, s50
	s_nop 0
	global_load_lds_dwordx4 v[242:243], off
	s_waitcnt vmcnt(8)
	s_waitcnt lgkmcnt(0)
	s_setprio 1
	s_barrier
	v_mfma_f32_16x16x32_bf16 v[56:59], v[132:135], v[190:193], 0
	v_mfma_f32_16x16x32_bf16 v[52:55], v[140:143], v[190:193], 0
	v_mfma_f32_16x16x32_bf16 v[40:43], v[132:135], v[198:201], 0
	v_mfma_f32_16x16x32_bf16 v[36:39], v[140:143], v[198:201], 0
	v_mfma_f32_16x16x32_bf16 v[24:27], v[132:135], v[222:225], 0
	v_mfma_f32_16x16x32_bf16 v[20:23], v[140:143], v[222:225], 0
	v_mfma_f32_16x16x32_bf16 v[8:11], v[132:135], v[230:233], 0
	v_mfma_f32_16x16x32_bf16 v[4:7], v[140:143], v[230:233], 0
	v_mfma_f32_16x16x32_bf16 v[56:59], v[136:139], v[194:197], v[56:59]
	v_mfma_f32_16x16x32_bf16 v[52:55], v[144:147], v[194:197], v[52:55]
	v_mfma_f32_16x16x32_bf16 v[40:43], v[136:139], v[202:205], v[40:43]
	v_mfma_f32_16x16x32_bf16 v[36:39], v[144:147], v[202:205], v[36:39]
	v_mfma_f32_16x16x32_bf16 v[24:27], v[136:139], v[226:229], v[24:27]
	v_mfma_f32_16x16x32_bf16 v[20:23], v[144:147], v[226:229], v[20:23]
	v_mfma_f32_16x16x32_bf16 v[8:11], v[136:139], v[234:237], v[8:11]
	v_mfma_f32_16x16x32_bf16 v[4:7], v[144:147], v[234:237], v[4:7]
	v_mfma_f32_16x16x32_bf16 v[64:67], v[148:151], v[190:193], 0
	v_mfma_f32_16x16x32_bf16 v[60:63], v[178:181], v[190:193], 0
	v_mfma_f32_16x16x32_bf16 v[48:51], v[148:151], v[198:201], 0
	v_mfma_f32_16x16x32_bf16 v[44:47], v[178:181], v[198:201], 0
	v_mfma_f32_16x16x32_bf16 v[32:35], v[148:151], v[222:225], 0
	v_mfma_f32_16x16x32_bf16 v[28:31], v[178:181], v[222:225], 0
	v_mfma_f32_16x16x32_bf16 v[16:19], v[148:151], v[230:233], 0
	v_mfma_f32_16x16x32_bf16 v[12:15], v[178:181], v[230:233], 0
	v_mfma_f32_16x16x32_bf16 v[64:67], v[152:155], v[194:197], v[64:67]
	v_mfma_f32_16x16x32_bf16 v[60:63], v[186:189], v[194:197], v[60:63]
	v_mfma_f32_16x16x32_bf16 v[48:51], v[152:155], v[202:205], v[48:51]
	v_mfma_f32_16x16x32_bf16 v[44:47], v[186:189], v[202:205], v[44:47]
	v_mfma_f32_16x16x32_bf16 v[32:35], v[152:155], v[226:229], v[32:35]
	v_mfma_f32_16x16x32_bf16 v[28:31], v[186:189], v[226:229], v[28:31]
	v_mfma_f32_16x16x32_bf16 v[16:19], v[152:155], v[234:237], v[16:19]
	v_mfma_f32_16x16x32_bf16 v[12:15], v[186:189], v[234:237], v[12:15]
	s_barrier
	s_setprio 0
	s_add_i32 s28, 0, 0x18000
	s_add_i32 s29, 0, 0x1c000
	v_add_u32_e32 v144, s28, v163
	v_add_u32_e32 v185, s29, v163
	ds_read_b128 v[132:135], v144
	ds_read_b128 v[136:139], v144 offset:1024
	ds_read_b128 v[140:143], v144 offset:2048
	ds_read_b128 v[144:147], v144 offset:3072
	ds_read_b128 v[148:151], v185
	ds_read_b128 v[152:155], v185 offset:1024
	ds_read_b128 v[178:181], v185 offset:2048
	ds_read_b128 v[186:189], v185 offset:3072
	s_add_u32 s26, s26, 0x100000
	s_addc_u32 s27, s27, 0
	s_mov_b32 m0, s51
	v_lshl_add_u64 v[244:245], s[26:27], 0, v[172:173]
	ds_read_b128 v[190:193], v184 offset:32768
	ds_read_b128 v[194:197], v184 offset:33792
	ds_read_b128 v[198:201], v184 offset:34816
	ds_read_b128 v[202:205], v184 offset:35840
	ds_read_b128 v[222:225], v184 offset:36864
	ds_read_b128 v[226:229], v184 offset:37888
	ds_read_b128 v[230:233], v184 offset:38912
	ds_read_b128 v[234:237], v184 offset:39936
	global_load_lds_dwordx4 v[244:245], off
	v_lshl_add_u64 v[244:245], s[26:27], 0, v[170:171]
	s_mov_b32 m0, s54
	s_nop 0
	global_load_lds_dwordx4 v[244:245], off
	s_waitcnt vmcnt(8)
	s_waitcnt lgkmcnt(0)
	s_setprio 1
	s_barrier
	v_mfma_f32_16x16x32_bf16 v[120:123], v[132:135], v[190:193], v[120:123]
	v_mfma_f32_16x16x32_bf16 v[116:119], v[140:143], v[190:193], v[116:119]
	v_mfma_f32_16x16x32_bf16 v[104:107], v[132:135], v[198:201], v[104:107]
	v_mfma_f32_16x16x32_bf16 v[100:103], v[140:143], v[198:201], v[100:103]
	v_mfma_f32_16x16x32_bf16 v[88:91], v[132:135], v[222:225], v[88:91]
	v_mfma_f32_16x16x32_bf16 v[84:87], v[140:143], v[222:225], v[84:87]
	v_mfma_f32_16x16x32_bf16 v[72:75], v[132:135], v[230:233], v[72:75]
	v_mfma_f32_16x16x32_bf16 v[68:71], v[140:143], v[230:233], v[68:71]
	v_mfma_f32_16x16x32_bf16 v[120:123], v[136:139], v[194:197], v[120:123]
	v_mfma_f32_16x16x32_bf16 v[116:119], v[144:147], v[194:197], v[116:119]
	v_mfma_f32_16x16x32_bf16 v[104:107], v[136:139], v[202:205], v[104:107]
	v_mfma_f32_16x16x32_bf16 v[100:103], v[144:147], v[202:205], v[100:103]
	v_mfma_f32_16x16x32_bf16 v[88:91], v[136:139], v[226:229], v[88:91]
	v_mfma_f32_16x16x32_bf16 v[84:87], v[144:147], v[226:229], v[84:87]
	v_mfma_f32_16x16x32_bf16 v[72:75], v[136:139], v[234:237], v[72:75]
	v_mfma_f32_16x16x32_bf16 v[68:71], v[144:147], v[234:237], v[68:71]
	v_mfma_f32_16x16x32_bf16 v[128:131], v[148:151], v[190:193], v[128:131]
	v_mfma_f32_16x16x32_bf16 v[124:127], v[178:181], v[190:193], v[124:127]
	v_mfma_f32_16x16x32_bf16 v[112:115], v[148:151], v[198:201], v[112:115]
	v_mfma_f32_16x16x32_bf16 v[108:111], v[178:181], v[198:201], v[108:111]
	v_mfma_f32_16x16x32_bf16 v[96:99], v[148:151], v[222:225], v[96:99]
	v_mfma_f32_16x16x32_bf16 v[92:95], v[178:181], v[222:225], v[92:95]
	v_mfma_f32_16x16x32_bf16 v[80:83], v[148:151], v[230:233], v[80:83]
	v_mfma_f32_16x16x32_bf16 v[76:79], v[178:181], v[230:233], v[76:79]
	v_mfma_f32_16x16x32_bf16 v[128:131], v[152:155], v[194:197], v[128:131]
	v_mfma_f32_16x16x32_bf16 v[124:127], v[186:189], v[194:197], v[124:127]
	v_mfma_f32_16x16x32_bf16 v[112:115], v[152:155], v[202:205], v[112:115]
	v_mfma_f32_16x16x32_bf16 v[108:111], v[186:189], v[202:205], v[108:111]
	v_mfma_f32_16x16x32_bf16 v[96:99], v[152:155], v[226:229], v[96:99]
	v_mfma_f32_16x16x32_bf16 v[92:95], v[186:189], v[226:229], v[92:95]
	v_mfma_f32_16x16x32_bf16 v[80:83], v[152:155], v[234:237], v[80:83]
	v_mfma_f32_16x16x32_bf16 v[76:79], v[186:189], v[234:237], v[76:79]
	s_barrier
	s_setprio 0
	s_add_i32 s26, s28, s1
	v_lshl_add_u64 v[182:183], v[182:183], 0, s[86:87]
	s_mov_b32 m0, s26
	ds_read_b128 v[190:193], v184 offset:49152
	ds_read_b128 v[194:197], v184 offset:50176
	ds_read_b128 v[198:201], v184 offset:51200
	ds_read_b128 v[202:205], v184 offset:52224
	ds_read_b128 v[222:225], v184 offset:53248
	ds_read_b128 v[226:229], v184 offset:54272
	ds_read_b128 v[230:233], v184 offset:55296
	ds_read_b128 v[234:237], v184 offset:56320
	global_load_lds_dwordx4 v[182:183], off
	s_add_i32 m0, s26, 0x2000
	s_add_u32 s24, s24, 0x100080
	v_lshl_add_u64 v[182:183], v[238:239], 0, s[86:87]
	s_addc_u32 s25, s25, 0
	s_add_i32 s26, s29, s1
	global_load_lds_dwordx4 v[182:183], off
	v_lshl_add_u64 v[182:183], s[24:25], 0, v[2:3]
	s_mov_b32 m0, s26
	s_nop 0
	global_load_lds_dwordx4 v[182:183], off
	v_lshl_add_u64 v[182:183], s[24:25], 0, v[168:169]
	s_add_i32 m0, s26, 0x2000
	s_nop 0
	global_load_lds_dwordx4 v[182:183], off
	v_lshl_add_u64 v[182:183], v[240:241], 0, s[86:87]
	s_mov_b32 m0, s78
	s_nop 0
	global_load_lds_dwordx4 v[182:183], off
	v_lshl_add_u64 v[182:183], v[242:243], 0, s[86:87]
	s_mov_b32 m0, s85
	s_nop 0
	global_load_lds_dwordx4 v[182:183], off
	s_waitcnt vmcnt(8)
	s_waitcnt lgkmcnt(0)
	s_setprio 1
	s_barrier
	v_mfma_f32_16x16x32_bf16 v[56:59], v[132:135], v[190:193], v[56:59]
	v_mfma_f32_16x16x32_bf16 v[52:55], v[140:143], v[190:193], v[52:55]
	v_mfma_f32_16x16x32_bf16 v[40:43], v[132:135], v[198:201], v[40:43]
	v_mfma_f32_16x16x32_bf16 v[36:39], v[140:143], v[198:201], v[36:39]
	v_mfma_f32_16x16x32_bf16 v[24:27], v[132:135], v[222:225], v[24:27]
	v_mfma_f32_16x16x32_bf16 v[20:23], v[140:143], v[222:225], v[20:23]
	v_mfma_f32_16x16x32_bf16 v[8:11], v[132:135], v[230:233], v[8:11]
	v_mfma_f32_16x16x32_bf16 v[4:7], v[140:143], v[230:233], v[4:7]
	v_mfma_f32_16x16x32_bf16 v[56:59], v[136:139], v[194:197], v[56:59]
	v_mfma_f32_16x16x32_bf16 v[52:55], v[144:147], v[194:197], v[52:55]
	v_mfma_f32_16x16x32_bf16 v[40:43], v[136:139], v[202:205], v[40:43]
	v_mfma_f32_16x16x32_bf16 v[36:39], v[144:147], v[202:205], v[36:39]
	v_mfma_f32_16x16x32_bf16 v[24:27], v[136:139], v[226:229], v[24:27]
	v_mfma_f32_16x16x32_bf16 v[20:23], v[144:147], v[226:229], v[20:23]
	v_mfma_f32_16x16x32_bf16 v[8:11], v[136:139], v[234:237], v[8:11]
	v_mfma_f32_16x16x32_bf16 v[4:7], v[144:147], v[234:237], v[4:7]
	v_mfma_f32_16x16x32_bf16 v[64:67], v[148:151], v[190:193], v[64:67]
	v_mfma_f32_16x16x32_bf16 v[60:63], v[178:181], v[190:193], v[60:63]
	v_mfma_f32_16x16x32_bf16 v[48:51], v[148:151], v[198:201], v[48:51]
	v_mfma_f32_16x16x32_bf16 v[44:47], v[178:181], v[198:201], v[44:47]
	v_mfma_f32_16x16x32_bf16 v[32:35], v[148:151], v[222:225], v[32:35]
	v_mfma_f32_16x16x32_bf16 v[28:31], v[178:181], v[222:225], v[28:31]
	v_mfma_f32_16x16x32_bf16 v[16:19], v[148:151], v[230:233], v[16:19]
	v_mfma_f32_16x16x32_bf16 v[12:15], v[178:181], v[230:233], v[12:15]
	v_mfma_f32_16x16x32_bf16 v[64:67], v[152:155], v[194:197], v[64:67]
	v_mfma_f32_16x16x32_bf16 v[60:63], v[186:189], v[194:197], v[60:63]
	v_mfma_f32_16x16x32_bf16 v[48:51], v[152:155], v[202:205], v[48:51]
	v_mfma_f32_16x16x32_bf16 v[44:47], v[186:189], v[202:205], v[44:47]
	v_mfma_f32_16x16x32_bf16 v[32:35], v[152:155], v[226:229], v[32:35]
	v_mfma_f32_16x16x32_bf16 v[28:31], v[186:189], v[226:229], v[28:31]
	v_mfma_f32_16x16x32_bf16 v[16:19], v[152:155], v[234:237], v[16:19]
	v_mfma_f32_16x16x32_bf16 v[12:15], v[186:189], v[234:237], v[12:15]
	s_barrier
	s_setprio 0
	s_add_i32 s58, s58, 2
	s_add_u32 s6, s6, 0x100
	s_addc_u32 s7, s7, 0
	s_add_u32 s21, s21, 0x100
	s_addc_u32 s13, s13, 0
	s_cmp_gt_u32 s58, 61
	s_cbranch_scc0 .LBB0_265

.LBB0_1201:
	s_ashr_i32 s53, s52, 31
	s_lshl_b64 s[26:27], s[52:53], 21
	s_add_u32 s72, s38, s26
	s_addc_u32 s73, s40, s27
	s_and_b64 s[26:27], s[4:5], exec
	s_cselect_b32 s35, s73, s7
	s_cselect_b32 s53, s72, s6
	s_ashr_i32 s31, s30, 31
	s_lshl_b64 s[26:27], s[30:31], 21
	s_add_u32 s74, s42, s26
	s_addc_u32 s75, s44, s27
	s_and_b64 s[26:27], s[4:5], exec
	s_cselect_b32 s31, s75, s25
	s_cselect_b32 s92, s74, s24
	s_add_u32 s6, s6, 0x100080
	s_addc_u32 s7, s7, 0
	s_add_u32 s21, s24, 0x100
	s_addc_u32 s13, s25, 0
	s_mov_b32 s58, -2
	s_waitcnt lgkmcnt(0)
	s_add_u32 s24, s6, 0xfff00080
	s_addc_u32 s25, s7, -1
	s_add_i32 s28, 0, 0x10000
	s_cmp_eq_u32 s58, 60
	s_cselect_b32 s27, s35, s25
	s_cselect_b32 s26, s53, s24
	s_cselect_b32 s25, s31, s13
	s_cselect_b32 s24, s92, s21
	s_add_i32 s71, 0, 0x14000
	v_add_u32_e32 v150, s28, v163
	v_add_u32_e32 v154, s71, v163
	ds_read_b128 v[138:141], v150
	ds_read_b128 v[142:145], v150 offset:1024
	ds_read_b128 v[146:149], v150 offset:2048
	ds_read_b128 v[150:153], v150 offset:3072
	ds_read_b128 v[168:171], v154
	ds_read_b128 v[172:175], v154 offset:1024
	ds_read_b128 v[176:179], v154 offset:2048
	ds_read_b128 v[180:183], v154 offset:3072
	v_lshl_add_u64 v[154:155], s[6:7], 0, v[134:135]
	s_add_i32 m0, s50, 0xc000
	ds_read_b128 v[188:191], v186
	ds_read_b128 v[192:195], v186 offset:1024
	ds_read_b128 v[196:199], v186 offset:2048
	ds_read_b128 v[200:203], v186 offset:3072
	ds_read_b128 v[222:225], v186 offset:4096
	ds_read_b128 v[226:229], v186 offset:5120
	ds_read_b128 v[230:233], v186 offset:6144
	ds_read_b128 v[234:237], v186 offset:7168
	global_load_lds_dwordx4 v[154:155], off
	v_lshl_add_u64 v[154:155], s[6:7], 0, v[136:137]
	s_add_i32 m0, s50, 0xe000
	s_nop 0
	global_load_lds_dwordx4 v[154:155], off
	s_waitcnt vmcnt(8)
	s_waitcnt lgkmcnt(0)
	s_setprio 1
	s_barrier
	v_mfma_f32_16x16x32_bf16 v[128:131], v[138:141], v[188:191], 0
	v_mfma_f32_16x16x32_bf16 v[124:127], v[146:149], v[188:191], 0
	v_mfma_f32_16x16x32_bf16 v[112:115], v[138:141], v[196:199], 0
	v_mfma_f32_16x16x32_bf16 v[108:111], v[146:149], v[196:199], 0
	v_mfma_f32_16x16x32_bf16 v[96:99], v[138:141], v[222:225], 0
	v_mfma_f32_16x16x32_bf16 v[92:95], v[146:149], v[222:225], 0
	v_mfma_f32_16x16x32_bf16 v[80:83], v[138:141], v[230:233], 0
	v_mfma_f32_16x16x32_bf16 v[76:79], v[146:149], v[230:233], 0
	v_mfma_f32_16x16x32_bf16 v[128:131], v[142:145], v[192:195], v[128:131]
	v_mfma_f32_16x16x32_bf16 v[124:127], v[150:153], v[192:195], v[124:127]
	v_mfma_f32_16x16x32_bf16 v[112:115], v[142:145], v[200:203], v[112:115]
	v_mfma_f32_16x16x32_bf16 v[108:111], v[150:153], v[200:203], v[108:111]
	v_mfma_f32_16x16x32_bf16 v[96:99], v[142:145], v[226:229], v[96:99]
	v_mfma_f32_16x16x32_bf16 v[92:95], v[150:153], v[226:229], v[92:95]
	v_mfma_f32_16x16x32_bf16 v[80:83], v[142:145], v[234:237], v[80:83]
	v_mfma_f32_16x16x32_bf16 v[76:79], v[150:153], v[234:237], v[76:79]
	v_mfma_f32_16x16x32_bf16 v[120:123], v[168:171], v[188:191], 0
	v_mfma_f32_16x16x32_bf16 v[116:119], v[176:179], v[188:191], 0
	v_mfma_f32_16x16x32_bf16 v[104:107], v[168:171], v[196:199], 0
	v_mfma_f32_16x16x32_bf16 v[100:103], v[176:179], v[196:199], 0
	v_mfma_f32_16x16x32_bf16 v[88:91], v[168:171], v[222:225], 0
	v_mfma_f32_16x16x32_bf16 v[84:87], v[176:179], v[222:225], 0
	v_mfma_f32_16x16x32_bf16 v[72:75], v[168:171], v[230:233], 0
	v_mfma_f32_16x16x32_bf16 v[68:71], v[176:179], v[230:233], 0
	v_mfma_f32_16x16x32_bf16 v[120:123], v[172:175], v[192:195], v[120:123]
	v_mfma_f32_16x16x32_bf16 v[116:119], v[180:183], v[192:195], v[116:119]
	v_mfma_f32_16x16x32_bf16 v[104:107], v[172:175], v[200:203], v[104:107]
	v_mfma_f32_16x16x32_bf16 v[100:103], v[180:183], v[200:203], v[100:103]
	v_mfma_f32_16x16x32_bf16 v[88:91], v[172:175], v[226:229], v[88:91]
	v_mfma_f32_16x16x32_bf16 v[84:87], v[180:183], v[226:229], v[84:87]
	v_mfma_f32_16x16x32_bf16 v[72:75], v[172:175], v[234:237], v[72:75]
	v_mfma_f32_16x16x32_bf16 v[68:71], v[180:183], v[234:237], v[68:71]
	s_barrier
	s_setprio 0
	s_add_i32 s28, s28, s46
	v_lshl_add_u64 v[154:155], s[24:25], 0, v[2:3]
	s_mov_b32 m0, s28
	ds_read_b128 v[188:191], v186 offset:16384
	ds_read_b128 v[192:195], v186 offset:17408
	ds_read_b128 v[196:199], v186 offset:18432
	ds_read_b128 v[200:203], v186 offset:19456
	ds_read_b128 v[222:225], v186 offset:20480
	ds_read_b128 v[226:229], v186 offset:21504
	ds_read_b128 v[230:233], v186 offset:22528
	ds_read_b128 v[234:237], v186 offset:23552
	global_load_lds_dwordx4 v[154:155], off
	s_add_i32 m0, s28, 0x2000
	s_add_u32 s28, s24, 0x100000
	v_lshl_add_u64 v[184:185], s[24:25], 0, v[132:133]
	s_addc_u32 s29, s25, 0
	s_add_i32 s71, s71, s46
	global_load_lds_dwordx4 v[184:185], off
	v_lshl_add_u64 v[204:205], s[28:29], 0, v[2:3]
	s_mov_b32 m0, s71
	v_lshl_add_u64 v[238:239], s[26:27], 0, v[132:133]
	global_load_lds_dwordx4 v[204:205], off
	v_lshl_add_u64 v[204:205], s[28:29], 0, v[132:133]
	s_add_i32 m0, s71, 0x2000
	s_nop 0
	global_load_lds_dwordx4 v[204:205], off
	v_lshl_add_u64 v[204:205], s[26:27], 0, v[2:3]
	s_mov_b32 m0, s50
	s_nop 0
	global_load_lds_dwordx4 v[204:205], off
	s_mov_b32 m0, s23
	s_nop 0
	global_load_lds_dwordx4 v[238:239], off
	s_waitcnt vmcnt(8)
	s_waitcnt lgkmcnt(0)
	s_setprio 1
	s_barrier
	v_mfma_f32_16x16x32_bf16 v[64:67], v[138:141], v[188:191], 0
	v_mfma_f32_16x16x32_bf16 v[60:63], v[146:149], v[188:191], 0
	v_mfma_f32_16x16x32_bf16 v[48:51], v[138:141], v[196:199], 0
	v_mfma_f32_16x16x32_bf16 v[44:47], v[146:149], v[196:199], 0
	v_mfma_f32_16x16x32_bf16 v[32:35], v[138:141], v[222:225], 0
	v_mfma_f32_16x16x32_bf16 v[28:31], v[146:149], v[222:225], 0
	v_mfma_f32_16x16x32_bf16 v[16:19], v[138:141], v[230:233], 0
	v_mfma_f32_16x16x32_bf16 v[12:15], v[146:149], v[230:233], 0
	v_mfma_f32_16x16x32_bf16 v[64:67], v[142:145], v[192:195], v[64:67]
	v_mfma_f32_16x16x32_bf16 v[60:63], v[150:153], v[192:195], v[60:63]
	v_mfma_f32_16x16x32_bf16 v[48:51], v[142:145], v[200:203], v[48:51]
	v_mfma_f32_16x16x32_bf16 v[44:47], v[150:153], v[200:203], v[44:47]
	v_mfma_f32_16x16x32_bf16 v[32:35], v[142:145], v[226:229], v[32:35]
	v_mfma_f32_16x16x32_bf16 v[28:31], v[150:153], v[226:229], v[28:31]
	v_mfma_f32_16x16x32_bf16 v[16:19], v[142:145], v[234:237], v[16:19]
	v_mfma_f32_16x16x32_bf16 v[12:15], v[150:153], v[234:237], v[12:15]
	v_mfma_f32_16x16x32_bf16 v[56:59], v[168:171], v[188:191], 0
	v_mfma_f32_16x16x32_bf16 v[52:55], v[176:179], v[188:191], 0
	v_mfma_f32_16x16x32_bf16 v[40:43], v[168:171], v[196:199], 0
	v_mfma_f32_16x16x32_bf16 v[36:39], v[176:179], v[196:199], 0
	v_mfma_f32_16x16x32_bf16 v[24:27], v[168:171], v[222:225], 0
	v_mfma_f32_16x16x32_bf16 v[20:23], v[176:179], v[222:225], 0
	v_mfma_f32_16x16x32_bf16 v[8:11], v[168:171], v[230:233], 0
	v_mfma_f32_16x16x32_bf16 v[4:7], v[176:179], v[230:233], 0
	v_mfma_f32_16x16x32_bf16 v[56:59], v[172:175], v[192:195], v[56:59]
	v_mfma_f32_16x16x32_bf16 v[52:55], v[180:183], v[192:195], v[52:55]
	v_mfma_f32_16x16x32_bf16 v[40:43], v[172:175], v[200:203], v[40:43]
	v_mfma_f32_16x16x32_bf16 v[36:39], v[180:183], v[200:203], v[36:39]
	v_mfma_f32_16x16x32_bf16 v[24:27], v[172:175], v[226:229], v[24:27]
	v_mfma_f32_16x16x32_bf16 v[20:23], v[180:183], v[226:229], v[20:23]
	v_mfma_f32_16x16x32_bf16 v[8:11], v[172:175], v[234:237], v[8:11]
	v_mfma_f32_16x16x32_bf16 v[4:7], v[180:183], v[234:237], v[4:7]
	s_barrier
	s_setprio 0
	s_add_i32 s28, 0, 0x18000
	s_add_i32 s29, 0, 0x1c000
	v_add_u32_e32 v150, s28, v163
	v_add_u32_e32 v180, s29, v163
	ds_read_b128 v[138:141], v150
	ds_read_b128 v[142:145], v150 offset:1024
	ds_read_b128 v[146:149], v150 offset:2048
	ds_read_b128 v[150:153], v150 offset:3072
	ds_read_b128 v[168:171], v180
	ds_read_b128 v[172:175], v180 offset:1024
	ds_read_b128 v[176:179], v180 offset:2048
	ds_read_b128 v[180:183], v180 offset:3072
	s_add_u32 s26, s26, 0x100000
	s_addc_u32 s27, s27, 0
	s_mov_b32 m0, s51
	v_lshl_add_u64 v[240:241], s[26:27], 0, v[2:3]
	ds_read_b128 v[188:191], v186 offset:32768
	ds_read_b128 v[192:195], v186 offset:33792
	ds_read_b128 v[196:199], v186 offset:34816
	ds_read_b128 v[200:203], v186 offset:35840
	ds_read_b128 v[222:225], v186 offset:36864
	ds_read_b128 v[226:229], v186 offset:37888
	ds_read_b128 v[230:233], v186 offset:38912
	ds_read_b128 v[234:237], v186 offset:39936
	global_load_lds_dwordx4 v[240:241], off
	v_lshl_add_u64 v[240:241], s[26:27], 0, v[132:133]
	s_mov_b32 m0, s54
	s_nop 0
	global_load_lds_dwordx4 v[240:241], off
	s_waitcnt vmcnt(8)
	s_waitcnt lgkmcnt(0)
	s_setprio 1
	s_barrier
	v_mfma_f32_16x16x32_bf16 v[128:131], v[138:141], v[188:191], v[128:131]
	v_mfma_f32_16x16x32_bf16 v[124:127], v[146:149], v[188:191], v[124:127]
	v_mfma_f32_16x16x32_bf16 v[112:115], v[138:141], v[196:199], v[112:115]
	v_mfma_f32_16x16x32_bf16 v[108:111], v[146:149], v[196:199], v[108:111]
	v_mfma_f32_16x16x32_bf16 v[96:99], v[138:141], v[222:225], v[96:99]
	v_mfma_f32_16x16x32_bf16 v[92:95], v[146:149], v[222:225], v[92:95]
	v_mfma_f32_16x16x32_bf16 v[80:83], v[138:141], v[230:233], v[80:83]
	v_mfma_f32_16x16x32_bf16 v[76:79], v[146:149], v[230:233], v[76:79]
	v_mfma_f32_16x16x32_bf16 v[128:131], v[142:145], v[192:195], v[128:131]
	v_mfma_f32_16x16x32_bf16 v[124:127], v[150:153], v[192:195], v[124:127]
	v_mfma_f32_16x16x32_bf16 v[112:115], v[142:145], v[200:203], v[112:115]
	v_mfma_f32_16x16x32_bf16 v[108:111], v[150:153], v[200:203], v[108:111]
	v_mfma_f32_16x16x32_bf16 v[96:99], v[142:145], v[226:229], v[96:99]
	v_mfma_f32_16x16x32_bf16 v[92:95], v[150:153], v[226:229], v[92:95]
	v_mfma_f32_16x16x32_bf16 v[80:83], v[142:145], v[234:237], v[80:83]
	v_mfma_f32_16x16x32_bf16 v[76:79], v[150:153], v[234:237], v[76:79]
	v_mfma_f32_16x16x32_bf16 v[120:123], v[168:171], v[188:191], v[120:123]
	v_mfma_f32_16x16x32_bf16 v[116:119], v[176:179], v[188:191], v[116:119]
	v_mfma_f32_16x16x32_bf16 v[104:107], v[168:171], v[196:199], v[104:107]
	v_mfma_f32_16x16x32_bf16 v[100:103], v[176:179], v[196:199], v[100:103]
	v_mfma_f32_16x16x32_bf16 v[88:91], v[168:171], v[222:225], v[88:91]
	v_mfma_f32_16x16x32_bf16 v[84:87], v[176:179], v[222:225], v[84:87]
	v_mfma_f32_16x16x32_bf16 v[72:75], v[168:171], v[230:233], v[72:75]
	v_mfma_f32_16x16x32_bf16 v[68:71], v[176:179], v[230:233], v[68:71]
	v_mfma_f32_16x16x32_bf16 v[120:123], v[172:175], v[192:195], v[120:123]
	v_mfma_f32_16x16x32_bf16 v[116:119], v[180:183], v[192:195], v[116:119]
	v_mfma_f32_16x16x32_bf16 v[104:107], v[172:175], v[200:203], v[104:107]
	v_mfma_f32_16x16x32_bf16 v[100:103], v[180:183], v[200:203], v[100:103]
	v_mfma_f32_16x16x32_bf16 v[88:91], v[172:175], v[226:229], v[88:91]
	v_mfma_f32_16x16x32_bf16 v[84:87], v[180:183], v[226:229], v[84:87]
	v_mfma_f32_16x16x32_bf16 v[72:75], v[172:175], v[234:237], v[72:75]
	v_mfma_f32_16x16x32_bf16 v[68:71], v[180:183], v[234:237], v[68:71]
	s_barrier
	s_setprio 0
	s_add_i32 s26, s28, s46
	v_lshl_add_u64 v[154:155], v[154:155], 0, s[86:87]
	s_mov_b32 m0, s26
	ds_read_b128 v[188:191], v186 offset:49152
	ds_read_b128 v[192:195], v186 offset:50176
	ds_read_b128 v[196:199], v186 offset:51200
	ds_read_b128 v[200:203], v186 offset:52224
	ds_read_b128 v[222:225], v186 offset:53248
	ds_read_b128 v[226:229], v186 offset:54272
	ds_read_b128 v[230:233], v186 offset:55296
	ds_read_b128 v[234:237], v186 offset:56320
	global_load_lds_dwordx4 v[154:155], off
	s_add_i32 m0, s26, 0x2000
	s_add_u32 s24, s24, 0x100080
	v_lshl_add_u64 v[154:155], v[184:185], 0, s[86:87]
	s_addc_u32 s25, s25, 0
	s_add_i32 s26, s29, s46
	global_load_lds_dwordx4 v[154:155], off
	v_lshl_add_u64 v[154:155], s[24:25], 0, v[2:3]
	s_mov_b32 m0, s26
	s_nop 0
	global_load_lds_dwordx4 v[154:155], off
	v_lshl_add_u64 v[154:155], s[24:25], 0, v[132:133]
	s_add_i32 m0, s26, 0x2000
	s_nop 0
	global_load_lds_dwordx4 v[154:155], off
	v_lshl_add_u64 v[154:155], v[204:205], 0, s[86:87]
	s_mov_b32 m0, s76
	s_nop 0
	global_load_lds_dwordx4 v[154:155], off
	v_lshl_add_u64 v[154:155], v[238:239], 0, s[86:87]
	s_mov_b32 m0, s77
	s_nop 0
	global_load_lds_dwordx4 v[154:155], off
	s_waitcnt vmcnt(8)
	s_waitcnt lgkmcnt(0)
	s_setprio 1
	s_barrier
	v_mfma_f32_16x16x32_bf16 v[64:67], v[138:141], v[188:191], v[64:67]
	v_mfma_f32_16x16x32_bf16 v[60:63], v[146:149], v[188:191], v[60:63]
	v_mfma_f32_16x16x32_bf16 v[48:51], v[138:141], v[196:199], v[48:51]
	v_mfma_f32_16x16x32_bf16 v[44:47], v[146:149], v[196:199], v[44:47]
	v_mfma_f32_16x16x32_bf16 v[32:35], v[138:141], v[222:225], v[32:35]
	v_mfma_f32_16x16x32_bf16 v[28:31], v[146:149], v[222:225], v[28:31]
	v_mfma_f32_16x16x32_bf16 v[16:19], v[138:141], v[230:233], v[16:19]
	v_mfma_f32_16x16x32_bf16 v[12:15], v[146:149], v[230:233], v[12:15]
	v_mfma_f32_16x16x32_bf16 v[64:67], v[142:145], v[192:195], v[64:67]
	v_mfma_f32_16x16x32_bf16 v[60:63], v[150:153], v[192:195], v[60:63]
	v_mfma_f32_16x16x32_bf16 v[48:51], v[142:145], v[200:203], v[48:51]
	v_mfma_f32_16x16x32_bf16 v[44:47], v[150:153], v[200:203], v[44:47]
	v_mfma_f32_16x16x32_bf16 v[32:35], v[142:145], v[226:229], v[32:35]
	v_mfma_f32_16x16x32_bf16 v[28:31], v[150:153], v[226:229], v[28:31]
	v_mfma_f32_16x16x32_bf16 v[16:19], v[142:145], v[234:237], v[16:19]
	v_mfma_f32_16x16x32_bf16 v[12:15], v[150:153], v[234:237], v[12:15]
	v_mfma_f32_16x16x32_bf16 v[56:59], v[168:171], v[188:191], v[56:59]
	v_mfma_f32_16x16x32_bf16 v[52:55], v[176:179], v[188:191], v[52:55]
	v_mfma_f32_16x16x32_bf16 v[40:43], v[168:171], v[196:199], v[40:43]
	v_mfma_f32_16x16x32_bf16 v[36:39], v[176:179], v[196:199], v[36:39]
	v_mfma_f32_16x16x32_bf16 v[24:27], v[168:171], v[222:225], v[24:27]
	v_mfma_f32_16x16x32_bf16 v[20:23], v[176:179], v[222:225], v[20:23]
	v_mfma_f32_16x16x32_bf16 v[8:11], v[168:171], v[230:233], v[8:11]
	v_mfma_f32_16x16x32_bf16 v[4:7], v[176:179], v[230:233], v[4:7]
	v_mfma_f32_16x16x32_bf16 v[56:59], v[172:175], v[192:195], v[56:59]
	v_mfma_f32_16x16x32_bf16 v[52:55], v[180:183], v[192:195], v[52:55]
	v_mfma_f32_16x16x32_bf16 v[40:43], v[172:175], v[200:203], v[40:43]
	v_mfma_f32_16x16x32_bf16 v[36:39], v[180:183], v[200:203], v[36:39]
	v_mfma_f32_16x16x32_bf16 v[24:27], v[172:175], v[226:229], v[24:27]
	v_mfma_f32_16x16x32_bf16 v[20:23], v[180:183], v[226:229], v[20:23]
	v_mfma_f32_16x16x32_bf16 v[8:11], v[172:175], v[234:237], v[8:11]
	v_mfma_f32_16x16x32_bf16 v[4:7], v[180:183], v[234:237], v[4:7]
	s_barrier
	s_setprio 0
	s_add_i32 s58, s58, 2
	s_add_u32 s6, s6, 0x100
	s_addc_u32 s7, s7, 0
	s_add_u32 s21, s21, 0x100
	s_addc_u32 s13, s13, 0
	s_cmp_gt_u32 s58, 61
	s_cbranch_scc0 .LBB0_1202
